# OUT GEMM epilogue: residual x loads issued 4 row-groups ahead (was 1), counted waits
# speedup vs baseline: 1.0372x; 1.0012x over previous
; template <class Epi, class Sched, bool GATHER, bool ALIGN_EPI = true, bool SP2 = true, bool REMAP64 = false>
; __device__ __forceinline__ void gemm_phase(LAS unsigned char* lds, const bf16* Ag, const bf16* Btg, const int K, const Sched& S, const Epi& E) {
;     ...
;             const bool hi = RP && (fr >= 8); const int rsh = hi ? -8 : 0, citx = hi ? cit + 32 : cit;
;             typename Epi::Pre pq[2];
;             { const int r0_ = wr * 64 + fr; pq[0] = E.pre(cur, (r0_ < cur.nrows ? r0_ : cur.nrows - 1) + rsh, citx); }
; #pragma unroll
;             for (int gq = 0; gq < 8; ++gq) { const int ai = gq >> 2, m = gq & 3, r = ai * HALF + wr * 64 + m * 16 + fr;
;                 if (gq + 1 < 8) { const int rn = ((gq + 1) >> 2) * HALF + wr * 64 + ((gq + 1) & 3) * 16 + fr; pq[(gq + 1) & 1] = E.pre(cur, (rn < cur.nrows ? rn : cur.nrows - 1) + rsh, citx); }
;                 __builtin_amdgcn_sched_barrier(0);
;                 if (r < cur.nrows) { float v0[8], v1[8];
; #pragma unroll
;                     for (int i = 0; i < 4; ++i) { v0[i] = acc[ai][0][m][0][i]; v0[4 + i] = acc[ai][0][m][1][i]; v1[i] = acc[ai][1][m][0][i]; v1[4 + i] = acc[ai][1][m][1][i]; }
;                     if constexpr (RP) {
; #pragma unroll
;                         for (int i = 0; i < 8; ++i) { const float snd = hi ? v0[i] : v1[i];
;                             const float rcv = __builtin_bit_cast(float, __builtin_amdgcn_update_dpp(0, __builtin_bit_cast(int, snd), 0x128, 0xf, 0xf, false));
;                             if (hi) v0[i] = rcv; else v1[i] = rcv; } }
;                     E.post(cur, r + rsh, citx, v0, v1, pq[gq & 1]); }
;                 __builtin_amdgcn_sched_barrier(0); }
;             }
;     __device__ __forceinline__ Pre pre(const Unit& u, int r, int cit) const { const size_t off = (size_t)(u.arow0 + r) * D + u.pn * 256 + cit; return Pre{__builtin_nontemporal_load((const f32x4*)(x + off)), __builtin_nontemporal_load((const f32x4*)(x + off + 4)), __builtin_nontemporal_load((const f3 ...
;     __device__ __forceinline__ void post(const Unit& u, int r, int cit, const float* v0, const float* v1, const Pre& p) const {
;         const size_t off = (size_t)(u.arow0 + r) * D + u.pn * 256 + cit; float a[8], b[8];
; #pragma unroll
;         for (int i = 0; i < 4; ++i) { a[i] = p.a0[i] + v0[i]; a[4 + i] = p.a1[i] + v0[4 + i]; b[i] = p.b0[i] + v1[i]; b[4 + i] = p.b1[i] + v1[4 + i]; }
.LBB0_1249:
	v_add_u32_e32 v130, s8, v192
	v_ashrrev_i32_e32 v131, 31, v130
	s_lshl_b32 s44, s42, 8
	v_readlane_b32 s80, v247, 8
	s_ashr_i32 s45, s44, 31
	v_lshlrev_b64 v[130:131], 13, v[130:131]
	v_readlane_b32 s81, v247, 9
	s_lshl_b64 s[52:53], s[44:45], 2
	v_add_u32_e32 v204, s8, v191
	v_lshl_add_u64 v[130:131], s[80:81], 0, v[130:131]
	v_lshl_add_u64 v[130:131], v[130:131], 0, s[52:53]
	v_lshl_add_u64 v[130:131], v[130:131], 0, v[172:173]
	global_load_dwordx4 v[146:149], v[130:131], off offset:16 nt
	global_load_dwordx4 v[150:153], v[130:131], off nt
	v_lshl_add_u64 v[132:133], v[130:131], 0, s[22:23]
	v_add_co_u32_e32 v130, vcc, 0x10000, v130
	v_lshl_add_u64 v[188:189], v[174:175], 0, s[52:53]
	s_nop 0
	v_addc_co_u32_e32 v131, vcc, 0, v131, vcc
	global_load_dwordx4 v[154:157], v[130:131], off nt
	global_load_dwordx4 v[158:161], v[132:133], off offset:16 nt
	v_add_u32_e32 v130, v204, v193
	v_ashrrev_i32_e32 v131, 31, v130
	v_lshlrev_b64 v[130:131], 13, v[130:131]
	v_lshl_add_u64 v[138:139], v[188:189], 0, v[130:131]
	global_load_dwordx4 v[130:133], v[138:139], off offset:16 nt
	global_load_dwordx4 v[134:137], v[138:139], off nt
	v_lshl_add_u64 v[142:143], v[138:139], 0, s[22:23]
	v_add_co_u32_e32 v138, vcc, 0x10000, v138
	v_lshl_add_u64 v[186:187], s[44:45], 1, v[176:177]
	s_nop 0
	v_addc_co_u32_e32 v139, vcc, 0, v139, vcc
	global_load_dwordx4 v[138:141], v[138:139], off nt
	s_nop 0
	global_load_dwordx4 v[142:145], v[142:143], off offset:16 nt
	v_add_u32_e32 v203, v204, v171
	v_readlane_b32 s82, v247, 10
	v_readlane_b32 s83, v247, 11
	v_readlane_b32 s84, v247, 12
	v_readlane_b32 s85, v247, 13
	v_readlane_b32 s86, v247, 14
	v_readlane_b32 s87, v247, 15
	v_readlane_b32 s88, v247, 16
	v_readlane_b32 s89, v247, 17
	v_readlane_b32 s90, v247, 18
	v_readlane_b32 s91, v247, 19
	v_readlane_b32 s92, v247, 20
	v_readlane_b32 s93, v247, 21
	v_readlane_b32 s94, v247, 22
	v_readlane_b32 s95, v247, 23
	s_nop 1
	v_add_u32_e32 v210, v204, v194
	v_ashrrev_i32_e32 v211, 31, v210
	v_lshlrev_b64 v[210:211], 13, v[210:211]
	v_lshl_add_u64 v[218:219], v[188:189], 0, v[210:211]
	global_load_dwordx4 v[210:213], v[218:219], off offset:16 nt
	global_load_dwordx4 v[214:217], v[218:219], off nt
	v_lshl_add_u64 v[222:223], v[218:219], 0, s[22:23]
	v_add_co_u32_e32 v218, vcc, 0x10000, v218
	s_nop 1
	v_addc_co_u32_e32 v219, vcc, 0, v219, vcc
	global_load_dwordx4 v[218:221], v[218:219], off nt
	s_nop 0
	global_load_dwordx4 v[222:225], v[222:223], off offset:16 nt
	s_nop 1
	v_add_u32_e32 v226, v204, v195
	v_ashrrev_i32_e32 v227, 31, v226
	v_lshlrev_b64 v[226:227], 13, v[226:227]
	v_lshl_add_u64 v[234:235], v[188:189], 0, v[226:227]
	global_load_dwordx4 v[226:229], v[234:235], off offset:16 nt
	global_load_dwordx4 v[230:233], v[234:235], off nt
	v_lshl_add_u64 v[238:239], v[234:235], 0, s[22:23]
	v_add_co_u32_e32 v234, vcc, 0x10000, v234
	s_nop 1
	v_addc_co_u32_e32 v235, vcc, 0, v235, vcc
	global_load_dwordx4 v[234:237], v[234:235], off nt
	s_nop 0
	global_load_dwordx4 v[238:241], v[238:239], off offset:16 nt
	s_and_b64 vcc, exec, s[18:19]
	s_cbranch_vccz .LBB0_1251
	s_waitcnt vmcnt(12)
	v_cndmask_b32_e64 v205, v118, v126, s[0:1]
	v_mov_b32_e32 v206, v173
	s_nop 1
	v_mov_b32_dpp v206, v205 row_ror:8 row_mask:0xf bank_mask:0xf
	v_cndmask_b32_e64 v205, v119, v127, s[0:1]
	v_cndmask_b32_e64 v126, v126, v206, s[0:1]
	v_cndmask_b32_e64 v118, v206, v118, s[0:1]
	v_mov_b32_e32 v206, v173
	s_nop 0
	v_add_f32_e32 v126, v150, v126
	v_mov_b32_dpp v206, v205 row_ror:8 row_mask:0xf bank_mask:0xf
	v_cndmask_b32_e64 v205, v120, v128, s[0:1]
	v_cndmask_b32_e64 v127, v127, v206, s[0:1]
	v_cndmask_b32_e64 v119, v206, v119, s[0:1]
	v_mov_b32_e32 v206, v173
	v_add_f32_e32 v127, v151, v127
	s_nop 0
	v_mov_b32_dpp v206, v205 row_ror:8 row_mask:0xf bank_mask:0xf
	v_cndmask_b32_e64 v205, v121, v129, s[0:1]
	v_cndmask_b32_e64 v128, v128, v206, s[0:1]
	v_cndmask_b32_e64 v120, v206, v120, s[0:1]
	v_mov_b32_e32 v206, v173
	v_add_f32_e32 v128, v152, v128
	v_add_f32_e32 v120, v156, v120
	v_mov_b32_dpp v206, v205 row_ror:8 row_mask:0xf bank_mask:0xf
	v_cndmask_b32_e64 v205, v114, v122, s[0:1]
	v_cndmask_b32_e64 v129, v129, v206, s[0:1]
	v_cndmask_b32_e64 v121, v206, v121, s[0:1]
	v_mov_b32_e32 v206, v173
	v_add_f32_e32 v121, v157, v121
	s_nop 0
	v_mov_b32_dpp v206, v205 row_ror:8 row_mask:0xf bank_mask:0xf
	v_cndmask_b32_e64 v205, v115, v123, s[0:1]
	v_cndmask_b32_e64 v122, v122, v206, s[0:1]
	v_cndmask_b32_e64 v114, v206, v114, s[0:1]
	v_mov_b32_e32 v206, v173
	v_add_f32_e32 v150, v158, v114
	v_add_u32_e32 v114, s62, v203
	v_mov_b32_dpp v206, v205 row_ror:8 row_mask:0xf bank_mask:0xf
	v_cndmask_b32_e64 v205, v116, v124, s[0:1]
	v_cndmask_b32_e64 v123, v123, v206, s[0:1]
	v_cndmask_b32_e64 v115, v206, v115, s[0:1]
	v_mov_b32_e32 v206, v173
	v_add_f32_e32 v151, v159, v115
	v_ashrrev_i32_e32 v115, 31, v114
	v_mov_b32_dpp v206, v205 row_ror:8 row_mask:0xf bank_mask:0xf
	v_cndmask_b32_e64 v205, v117, v125, s[0:1]
	v_cndmask_b32_e64 v124, v124, v206, s[0:1]
	v_cndmask_b32_e64 v116, v206, v116, s[0:1]
	v_mov_b32_e32 v206, v173
	v_add_f32_e32 v122, v146, v122
	v_add_f32_e32 v123, v147, v123
	v_mov_b32_dpp v206, v205 row_ror:8 row_mask:0xf bank_mask:0xf
	v_cndmask_b32_e64 v125, v125, v206, s[0:1]
	v_cndmask_b32_e64 v117, v206, v117, s[0:1]
	v_add_f32_e32 v124, v148, v124
	v_add_f32_e32 v148, v160, v116
	v_add_f32_e32 v116, v153, v129
	v_add_f32_e32 v125, v149, v125
	v_lshlrev_b64 v[114:115], 12, v[114:115]
	v_add_f32_e32 v146, v154, v118
	v_add_f32_e32 v147, v155, v119
	v_add_f32_e32 v129, v161, v117
	v_lshl_add_u64 v[118:119], v[186:187], 0, v[114:115]
	v_cvt_pk_bf16_f32 v114, v126, v127
	v_cvt_pk_bf16_f32 v115, v128, v116
	v_cvt_pk_bf16_f32 v116, v122, v123
	v_cvt_pk_bf16_f32 v117, v124, v125
	global_store_dwordx4 v[118:119], v[114:117], off
	v_add_co_u32_e32 v118, vcc, 0x8000, v118
	s_nop 0
	v_cvt_pk_bf16_f32 v114, v146, v147
	v_cvt_pk_bf16_f32 v115, v120, v121
	v_cvt_pk_bf16_f32 v116, v150, v151
	v_cvt_pk_bf16_f32 v117, v148, v129
	v_addc_co_u32_e32 v119, vcc, 0, v119, vcc
	global_store_dwordx4 v[118:119], v[114:117], off
; template <class Epi, class Sched, bool GATHER, bool ALIGN_EPI = true, bool SP2 = true, bool REMAP64 = false>
; __device__ __forceinline__ void gemm_phase(LAS unsigned char* lds, const bf16* Ag, const bf16* Btg, const int K, const Sched& S, const Epi& E) {
;     ...
;             const bool hi = RP && (fr >= 8); const int rsh = hi ? -8 : 0, citx = hi ? cit + 32 : cit;
;             typename Epi::Pre pq[2];
;             { const int r0_ = wr * 64 + fr; pq[0] = E.pre(cur, (r0_ < cur.nrows ? r0_ : cur.nrows - 1) + rsh, citx); }
; #pragma unroll
;             for (int gq = 0; gq < 8; ++gq) { const int ai = gq >> 2, m = gq & 3, r = ai * HALF + wr * 64 + m * 16 + fr;
;                 if (gq + 1 < 8) { const int rn = ((gq + 1) >> 2) * HALF + wr * 64 + ((gq + 1) & 3) * 16 + fr; pq[(gq + 1) & 1] = E.pre(cur, (rn < cur.nrows ? rn : cur.nrows - 1) + rsh, citx); }
;                 __builtin_amdgcn_sched_barrier(0);
;                 if (r < cur.nrows) { float v0[8], v1[8];
; #pragma unroll
;                     for (int i = 0; i < 4; ++i) { v0[i] = acc[ai][0][m][0][i]; v0[4 + i] = acc[ai][0][m][1][i]; v1[i] = acc[ai][1][m][0][i]; v1[4 + i] = acc[ai][1][m][1][i]; }
;                     if constexpr (RP) {
; #pragma unroll
;                         for (int i = 0; i < 8; ++i) { const float snd = hi ? v0[i] : v1[i];
;                             const float rcv = __builtin_bit_cast(float, __builtin_amdgcn_update_dpp(0, __builtin_bit_cast(int, snd), 0x128, 0xf, 0xf, false));
;                             if (hi) v0[i] = rcv; else v1[i] = rcv; } }
;                     E.post(cur, r + rsh, citx, v0, v1, pq[gq & 1]); }
;                 __builtin_amdgcn_sched_barrier(0); }
;             }
;     __device__ __forceinline__ Pre pre(const Unit& u, int r, int cit) const { const size_t off = (size_t)(u.arow0 + r) * D + u.pn * 256 + cit; return Pre{__builtin_nontemporal_load((const f32x4*)(x + off)), __builtin_nontemporal_load((const f32x4*)(x + off + 4)), __builtin_nontemporal_load((const f3 ...
;     __device__ __forceinline__ void post(const Unit& u, int r, int cit, const float* v0, const float* v1, const Pre& p) const {
;         const size_t off = (size_t)(u.arow0 + r) * D + u.pn * 256 + cit; float a[8], b[8];
; #pragma unroll
;         for (int i = 0; i < 4; ++i) { a[i] = p.a0[i] + v0[i]; a[4 + i] = p.a1[i] + v0[4 + i]; b[i] = p.b0[i] + v1[i]; b[4 + i] = p.b1[i] + v1[4 + i]; }
.LBB0_1251:
	s_nop 1
	v_add_u32_e32 v114, v204, v196
	v_ashrrev_i32_e32 v115, 31, v114
	v_lshlrev_b64 v[114:115], 13, v[114:115]
	v_lshl_add_u64 v[122:123], v[188:189], 0, v[114:115]
	global_load_dwordx4 v[114:117], v[122:123], off offset:16 nt
	global_load_dwordx4 v[118:121], v[122:123], off nt
	v_lshl_add_u64 v[126:127], v[122:123], 0, s[22:23]
	v_add_co_u32_e32 v122, vcc, 0x10000, v122
	s_nop 1
	v_addc_co_u32_e32 v123, vcc, 0, v123, vcc
	global_load_dwordx4 v[122:125], v[122:123], off nt
	s_nop 0
	global_load_dwordx4 v[126:129], v[126:127], off offset:16 nt
	s_nop 0
	v_cndmask_b32_e64 v244, 0, 1, s[18:19]
	v_cmp_ne_u32_e64 s[8:9], 1, v244
	s_andn2_b64 vcc, exec, s[18:19]
	s_cbranch_vccnz .LBB0_1253
	s_waitcnt vmcnt(14)
	v_cndmask_b32_e64 v146, v102, v110, s[0:1]
	v_mov_b32_e32 v147, v173
	s_nop 1
	v_mov_b32_dpp v147, v146 row_ror:8 row_mask:0xf bank_mask:0xf
	v_cndmask_b32_e64 v146, v103, v111, s[0:1]
	v_cndmask_b32_e64 v110, v110, v147, s[0:1]
	v_cndmask_b32_e64 v102, v147, v102, s[0:1]
	v_mov_b32_e32 v147, v173
	v_add_f32_e32 v110, v134, v110
	s_nop 0
	v_mov_b32_dpp v147, v146 row_ror:8 row_mask:0xf bank_mask:0xf
	v_cndmask_b32_e64 v146, v104, v112, s[0:1]
	v_cndmask_b32_e64 v111, v111, v147, s[0:1]
	v_cndmask_b32_e64 v103, v147, v103, s[0:1]
	v_mov_b32_e32 v147, v173
	v_add_f32_e32 v111, v135, v111
	s_nop 0
	v_mov_b32_dpp v147, v146 row_ror:8 row_mask:0xf bank_mask:0xf
	v_cndmask_b32_e64 v146, v105, v113, s[0:1]
	v_cndmask_b32_e64 v112, v112, v147, s[0:1]
	v_cndmask_b32_e64 v104, v147, v104, s[0:1]
	v_mov_b32_e32 v147, v173
	v_add_f32_e32 v112, v136, v112
	v_add_f32_e32 v104, v140, v104
	v_mov_b32_dpp v147, v146 row_ror:8 row_mask:0xf bank_mask:0xf
	v_cndmask_b32_e64 v146, v98, v106, s[0:1]
	v_cndmask_b32_e64 v113, v113, v147, s[0:1]
	v_cndmask_b32_e64 v105, v147, v105, s[0:1]
	v_mov_b32_e32 v147, v173
	v_add_f32_e32 v105, v141, v105
	s_nop 0
	v_mov_b32_dpp v147, v146 row_ror:8 row_mask:0xf bank_mask:0xf
	v_cndmask_b32_e64 v146, v99, v107, s[0:1]
	v_cndmask_b32_e64 v106, v106, v147, s[0:1]
	v_cndmask_b32_e64 v98, v147, v98, s[0:1]
	v_mov_b32_e32 v147, v173
	v_add_f32_e32 v134, v142, v98
	v_add_u32_e32 v98, s65, v203
	v_mov_b32_dpp v147, v146 row_ror:8 row_mask:0xf bank_mask:0xf
	v_cndmask_b32_e64 v146, v100, v108, s[0:1]
	v_cndmask_b32_e64 v107, v107, v147, s[0:1]
	v_cndmask_b32_e64 v99, v147, v99, s[0:1]
	v_mov_b32_e32 v147, v173
	v_add_f32_e32 v135, v143, v99
	v_ashrrev_i32_e32 v99, 31, v98
	v_mov_b32_dpp v147, v146 row_ror:8 row_mask:0xf bank_mask:0xf
	v_cndmask_b32_e64 v146, v101, v109, s[0:1]
	v_cndmask_b32_e64 v108, v108, v147, s[0:1]
	v_cndmask_b32_e64 v100, v147, v100, s[0:1]
	v_mov_b32_e32 v147, v173
	v_add_f32_e32 v106, v130, v106
	v_add_f32_e32 v107, v131, v107
	v_mov_b32_dpp v147, v146 row_ror:8 row_mask:0xf bank_mask:0xf
	v_cndmask_b32_e64 v109, v109, v147, s[0:1]
	v_cndmask_b32_e64 v101, v147, v101, s[0:1]
	v_add_f32_e32 v108, v132, v108
	v_add_f32_e32 v132, v144, v100
	v_add_f32_e32 v100, v137, v113
	v_add_f32_e32 v109, v133, v109
	v_lshlrev_b64 v[98:99], 12, v[98:99]
	v_add_f32_e32 v130, v138, v102
	v_add_f32_e32 v131, v139, v103
	v_add_f32_e32 v113, v145, v101
	v_lshl_add_u64 v[102:103], v[186:187], 0, v[98:99]
	v_cvt_pk_bf16_f32 v98, v110, v111
	v_cvt_pk_bf16_f32 v99, v112, v100
	v_cvt_pk_bf16_f32 v100, v106, v107
	v_cvt_pk_bf16_f32 v101, v108, v109
	global_store_dwordx4 v[102:103], v[98:101], off
	v_add_co_u32_e32 v102, vcc, 0x8000, v102
	s_nop 0
	v_cvt_pk_bf16_f32 v98, v130, v131
	v_cvt_pk_bf16_f32 v99, v104, v105
	v_cvt_pk_bf16_f32 v100, v134, v135
	v_cvt_pk_bf16_f32 v101, v132, v113
	v_addc_co_u32_e32 v103, vcc, 0, v103, vcc
	global_store_dwordx4 v[102:103], v[98:101], off
.LBB0_1253:
	s_nop 1
	v_add_u32_e32 v98, v204, v197
	v_ashrrev_i32_e32 v99, 31, v98
	v_lshlrev_b64 v[98:99], 13, v[98:99]
	v_lshl_add_u64 v[106:107], v[188:189], 0, v[98:99]
	global_load_dwordx4 v[98:101], v[106:107], off offset:16 nt
	global_load_dwordx4 v[102:105], v[106:107], off nt
	v_lshl_add_u64 v[110:111], v[106:107], 0, s[22:23]
	v_add_co_u32_e32 v106, vcc, 0x10000, v106
	s_nop 1
	v_addc_co_u32_e32 v107, vcc, 0, v107, vcc
	global_load_dwordx4 v[106:109], v[106:107], off nt
	s_nop 0
	global_load_dwordx4 v[110:113], v[110:111], off offset:16 nt
	s_and_b64 vcc, exec, s[8:9]
	s_cbranch_vccnz .LBB0_1255
; template <class Epi, class Sched, bool GATHER, bool ALIGN_EPI = true, bool SP2 = true, bool REMAP64 = false>
; __device__ __forceinline__ void gemm_phase(LAS unsigned char* lds, const bf16* Ag, const bf16* Btg, const int K, const Sched& S, const Epi& E) {
;     ...
;             const bool hi = RP && (fr >= 8); const int rsh = hi ? -8 : 0, citx = hi ? cit + 32 : cit;
;             typename Epi::Pre pq[2];
;             { const int r0_ = wr * 64 + fr; pq[0] = E.pre(cur, (r0_ < cur.nrows ? r0_ : cur.nrows - 1) + rsh, citx); }
; #pragma unroll
;             for (int gq = 0; gq < 8; ++gq) { const int ai = gq >> 2, m = gq & 3, r = ai * HALF + wr * 64 + m * 16 + fr;
;                 if (gq + 1 < 8) { const int rn = ((gq + 1) >> 2) * HALF + wr * 64 + ((gq + 1) & 3) * 16 + fr; pq[(gq + 1) & 1] = E.pre(cur, (rn < cur.nrows ? rn : cur.nrows - 1) + rsh, citx); }
;                 __builtin_amdgcn_sched_barrier(0);
;                 if (r < cur.nrows) { float v0[8], v1[8];
; #pragma unroll
;                     for (int i = 0; i < 4; ++i) { v0[i] = acc[ai][0][m][0][i]; v0[4 + i] = acc[ai][0][m][1][i]; v1[i] = acc[ai][1][m][0][i]; v1[4 + i] = acc[ai][1][m][1][i]; }
;                     if constexpr (RP) {
; #pragma unroll
;                         for (int i = 0; i < 8; ++i) { const float snd = hi ? v0[i] : v1[i];
;                             const float rcv = __builtin_bit_cast(float, __builtin_amdgcn_update_dpp(0, __builtin_bit_cast(int, snd), 0x128, 0xf, 0xf, false));
;                             if (hi) v0[i] = rcv; else v1[i] = rcv; } }
;                     E.post(cur, r + rsh, citx, v0, v1, pq[gq & 1]); }
;                 __builtin_amdgcn_sched_barrier(0); }
;             }
;     __device__ __forceinline__ Pre pre(const Unit& u, int r, int cit) const { const size_t off = (size_t)(u.arow0 + r) * D + u.pn * 256 + cit; return Pre{__builtin_nontemporal_load((const f32x4*)(x + off)), __builtin_nontemporal_load((const f32x4*)(x + off + 4)), __builtin_nontemporal_load((const f3 ...
;     __device__ __forceinline__ void post(const Unit& u, int r, int cit, const float* v0, const float* v1, const Pre& p) const {
;         const size_t off = (size_t)(u.arow0 + r) * D + u.pn * 256 + cit; float a[8], b[8];
; #pragma unroll
;         for (int i = 0; i < 4; ++i) { a[i] = p.a0[i] + v0[i]; a[4 + i] = p.a1[i] + v0[4 + i]; b[i] = p.b0[i] + v1[i]; b[4 + i] = p.b1[i] + v1[4 + i]; }
	s_waitcnt vmcnt(16)
	v_cndmask_b32_e64 v130, v86, v94, s[0:1]
	v_mov_b32_e32 v131, v173
	s_nop 1
	v_mov_b32_dpp v131, v130 row_ror:8 row_mask:0xf bank_mask:0xf
	v_cndmask_b32_e64 v130, v87, v95, s[0:1]
	v_cndmask_b32_e64 v94, v94, v131, s[0:1]
	v_cndmask_b32_e64 v86, v131, v86, s[0:1]
	v_mov_b32_e32 v131, v173
	v_add_f32_e32 v94, v214, v94
	s_nop 0
	v_mov_b32_dpp v131, v130 row_ror:8 row_mask:0xf bank_mask:0xf
	v_cndmask_b32_e64 v130, v88, v96, s[0:1]
	v_cndmask_b32_e64 v95, v95, v131, s[0:1]
	v_cndmask_b32_e64 v87, v131, v87, s[0:1]
	v_mov_b32_e32 v131, v173
	v_add_f32_e32 v95, v215, v95
	s_nop 0
	v_mov_b32_dpp v131, v130 row_ror:8 row_mask:0xf bank_mask:0xf
	v_cndmask_b32_e64 v130, v89, v97, s[0:1]
	v_cndmask_b32_e64 v96, v96, v131, s[0:1]
	v_cndmask_b32_e64 v88, v131, v88, s[0:1]
	v_mov_b32_e32 v131, v173
	v_add_f32_e32 v96, v216, v96
	v_add_f32_e32 v88, v220, v88
	v_mov_b32_dpp v131, v130 row_ror:8 row_mask:0xf bank_mask:0xf
	v_cndmask_b32_e64 v130, v82, v90, s[0:1]
	v_cndmask_b32_e64 v97, v97, v131, s[0:1]
	v_cndmask_b32_e64 v89, v131, v89, s[0:1]
	v_mov_b32_e32 v131, v173
	v_add_f32_e32 v89, v221, v89
	s_nop 0
	v_mov_b32_dpp v131, v130 row_ror:8 row_mask:0xf bank_mask:0xf
	v_cndmask_b32_e64 v130, v83, v91, s[0:1]
	v_cndmask_b32_e64 v90, v90, v131, s[0:1]
	v_cndmask_b32_e64 v82, v131, v82, s[0:1]
	v_mov_b32_e32 v131, v173
	v_add_f32_e32 v214, v222, v82
	v_add_u32_e32 v82, s70, v203
	v_mov_b32_dpp v131, v130 row_ror:8 row_mask:0xf bank_mask:0xf
	v_cndmask_b32_e64 v130, v84, v92, s[0:1]
	v_cndmask_b32_e64 v91, v91, v131, s[0:1]
	v_cndmask_b32_e64 v83, v131, v83, s[0:1]
	v_mov_b32_e32 v131, v173
	v_add_f32_e32 v215, v223, v83
	v_ashrrev_i32_e32 v83, 31, v82
	v_mov_b32_dpp v131, v130 row_ror:8 row_mask:0xf bank_mask:0xf
	v_cndmask_b32_e64 v130, v85, v93, s[0:1]
	v_cndmask_b32_e64 v92, v92, v131, s[0:1]
	v_cndmask_b32_e64 v84, v131, v84, s[0:1]
	v_mov_b32_e32 v131, v173
	v_add_f32_e32 v90, v210, v90
	v_add_f32_e32 v91, v211, v91
	v_mov_b32_dpp v131, v130 row_ror:8 row_mask:0xf bank_mask:0xf
	v_cndmask_b32_e64 v93, v93, v131, s[0:1]
	v_cndmask_b32_e64 v85, v131, v85, s[0:1]
	v_add_f32_e32 v92, v212, v92
	v_add_f32_e32 v212, v224, v84
	v_add_f32_e32 v84, v217, v97
	v_add_f32_e32 v93, v213, v93
	v_lshlrev_b64 v[82:83], 12, v[82:83]
	v_add_f32_e32 v210, v218, v86
	v_add_f32_e32 v211, v219, v87
	v_add_f32_e32 v97, v225, v85
	v_lshl_add_u64 v[86:87], v[186:187], 0, v[82:83]
	v_cvt_pk_bf16_f32 v82, v94, v95
	v_cvt_pk_bf16_f32 v83, v96, v84
	v_cvt_pk_bf16_f32 v84, v90, v91
	v_cvt_pk_bf16_f32 v85, v92, v93
	global_store_dwordx4 v[86:87], v[82:85], off
	v_add_co_u32_e32 v86, vcc, 0x8000, v86
	s_nop 0
	v_cvt_pk_bf16_f32 v82, v210, v211
	v_cvt_pk_bf16_f32 v83, v88, v89
	v_cvt_pk_bf16_f32 v84, v214, v215
	v_cvt_pk_bf16_f32 v85, v212, v97
	v_addc_co_u32_e32 v87, vcc, 0, v87, vcc
	global_store_dwordx4 v[86:87], v[82:85], off
.LBB0_1255:
	s_nop 1
	v_add_u32_e32 v82, v204, v198
	v_ashrrev_i32_e32 v83, 31, v82
	v_lshlrev_b64 v[82:83], 13, v[82:83]
	v_lshl_add_u64 v[90:91], v[188:189], 0, v[82:83]
	global_load_dwordx4 v[82:85], v[90:91], off offset:16 nt
	global_load_dwordx4 v[86:89], v[90:91], off nt
	v_lshl_add_u64 v[94:95], v[90:91], 0, s[22:23]
	v_add_co_u32_e32 v90, vcc, 0x10000, v90
	s_nop 1
	v_addc_co_u32_e32 v91, vcc, 0, v91, vcc
	global_load_dwordx4 v[90:93], v[90:91], off nt
	s_nop 0
	global_load_dwordx4 v[94:97], v[94:95], off offset:16 nt
	s_and_b64 vcc, exec, s[8:9]
	s_cbranch_vccnz .LBB0_1257
	s_waitcnt vmcnt(18)
	v_cndmask_b32_e64 v242, v70, v78, s[0:1]
	v_mov_b32_e32 v243, v173
	s_nop 1
	v_mov_b32_dpp v243, v242 row_ror:8 row_mask:0xf bank_mask:0xf
	v_cndmask_b32_e64 v242, v71, v79, s[0:1]
	v_cndmask_b32_e64 v78, v78, v243, s[0:1]
	v_cndmask_b32_e64 v70, v243, v70, s[0:1]
	v_mov_b32_e32 v243, v173
	s_nop 0
	v_add_f32_e32 v78, v230, v78
	v_mov_b32_dpp v243, v242 row_ror:8 row_mask:0xf bank_mask:0xf
	v_cndmask_b32_e64 v242, v72, v80, s[0:1]
	v_cndmask_b32_e64 v79, v79, v243, s[0:1]
	v_cndmask_b32_e64 v71, v243, v71, s[0:1]
	v_mov_b32_e32 v243, v173
	v_add_f32_e32 v79, v231, v79
	s_nop 0
	v_mov_b32_dpp v243, v242 row_ror:8 row_mask:0xf bank_mask:0xf
	v_cndmask_b32_e64 v242, v73, v81, s[0:1]
	v_cndmask_b32_e64 v80, v80, v243, s[0:1]
	v_cndmask_b32_e64 v72, v243, v72, s[0:1]
	v_mov_b32_e32 v243, v173
	v_add_f32_e32 v80, v232, v80
	s_nop 0
	v_add_f32_e32 v72, v236, v72
	v_mov_b32_dpp v243, v242 row_ror:8 row_mask:0xf bank_mask:0xf
	v_cndmask_b32_e64 v242, v66, v74, s[0:1]
	v_cndmask_b32_e64 v81, v81, v243, s[0:1]
	v_cndmask_b32_e64 v73, v243, v73, s[0:1]
	v_mov_b32_e32 v243, v173
	v_add_f32_e32 v73, v237, v73
	s_nop 0
	v_mov_b32_dpp v243, v242 row_ror:8 row_mask:0xf bank_mask:0xf
	v_cndmask_b32_e64 v242, v67, v75, s[0:1]
	v_cndmask_b32_e64 v74, v74, v243, s[0:1]
	v_cndmask_b32_e64 v66, v243, v66, s[0:1]
	v_mov_b32_e32 v243, v173
	s_nop 0
	v_add_f32_e32 v230, v238, v66
	v_add_u32_e32 v66, s72, v203
	v_mov_b32_dpp v243, v242 row_ror:8 row_mask:0xf bank_mask:0xf
	v_cndmask_b32_e64 v242, v68, v76, s[0:1]
	v_cndmask_b32_e64 v75, v75, v243, s[0:1]
	v_cndmask_b32_e64 v67, v243, v67, s[0:1]
	v_mov_b32_e32 v243, v173
	v_add_f32_e32 v231, v239, v67
	v_ashrrev_i32_e32 v67, 31, v66
	v_mov_b32_dpp v243, v242 row_ror:8 row_mask:0xf bank_mask:0xf
	v_cndmask_b32_e64 v242, v69, v77, s[0:1]
	v_cndmask_b32_e64 v76, v76, v243, s[0:1]
	v_cndmask_b32_e64 v68, v243, v68, s[0:1]
	v_mov_b32_e32 v243, v173
	v_add_f32_e32 v74, v226, v74
	v_add_f32_e32 v75, v227, v75
	v_mov_b32_dpp v243, v242 row_ror:8 row_mask:0xf bank_mask:0xf
	v_cndmask_b32_e64 v77, v77, v243, s[0:1]
	v_cndmask_b32_e64 v69, v243, v69, s[0:1]
	v_add_f32_e32 v76, v228, v76
	v_add_f32_e32 v228, v240, v68
	v_add_f32_e32 v68, v233, v81
	v_add_f32_e32 v77, v229, v77
	v_lshlrev_b64 v[66:67], 12, v[66:67]
	v_add_f32_e32 v226, v234, v70
	v_add_f32_e32 v227, v235, v71
	v_add_f32_e32 v81, v241, v69
	v_lshl_add_u64 v[70:71], v[186:187], 0, v[66:67]
	v_cvt_pk_bf16_f32 v66, v78, v79
	v_cvt_pk_bf16_f32 v67, v80, v68
	v_cvt_pk_bf16_f32 v68, v74, v75
	v_cvt_pk_bf16_f32 v69, v76, v77
	global_store_dwordx4 v[70:71], v[66:69], off
	v_add_co_u32_e32 v70, vcc, 0x8000, v70
	s_nop 0
	v_cvt_pk_bf16_f32 v66, v226, v227
	v_cvt_pk_bf16_f32 v67, v72, v73
	v_cvt_pk_bf16_f32 v68, v230, v231
	v_cvt_pk_bf16_f32 v69, v228, v81
	v_addc_co_u32_e32 v71, vcc, 0, v71, vcc
	global_store_dwordx4 v[70:71], v[66:69], off
; template <class Epi, class Sched, bool GATHER, bool ALIGN_EPI = true, bool SP2 = true, bool REMAP64 = false>
; __device__ __forceinline__ void gemm_phase(LAS unsigned char* lds, const bf16* Ag, const bf16* Btg, const int K, const Sched& S, const Epi& E) {
;     ...
;             const bool hi = RP && (fr >= 8); const int rsh = hi ? -8 : 0, citx = hi ? cit + 32 : cit;
;             typename Epi::Pre pq[2];
;             { const int r0_ = wr * 64 + fr; pq[0] = E.pre(cur, (r0_ < cur.nrows ? r0_ : cur.nrows - 1) + rsh, citx); }
; #pragma unroll
;             for (int gq = 0; gq < 8; ++gq) { const int ai = gq >> 2, m = gq & 3, r = ai * HALF + wr * 64 + m * 16 + fr;
;                 if (gq + 1 < 8) { const int rn = ((gq + 1) >> 2) * HALF + wr * 64 + ((gq + 1) & 3) * 16 + fr; pq[(gq + 1) & 1] = E.pre(cur, (rn < cur.nrows ? rn : cur.nrows - 1) + rsh, citx); }
;                 __builtin_amdgcn_sched_barrier(0);
;                 if (r < cur.nrows) { float v0[8], v1[8];
; #pragma unroll
;                     for (int i = 0; i < 4; ++i) { v0[i] = acc[ai][0][m][0][i]; v0[4 + i] = acc[ai][0][m][1][i]; v1[i] = acc[ai][1][m][0][i]; v1[4 + i] = acc[ai][1][m][1][i]; }
;                     if constexpr (RP) {
; #pragma unroll
;                         for (int i = 0; i < 8; ++i) { const float snd = hi ? v0[i] : v1[i];
;                             const float rcv = __builtin_bit_cast(float, __builtin_amdgcn_update_dpp(0, __builtin_bit_cast(int, snd), 0x128, 0xf, 0xf, false));
;                             if (hi) v0[i] = rcv; else v1[i] = rcv; } }
;                     E.post(cur, r + rsh, citx, v0, v1, pq[gq & 1]); }
;                 __builtin_amdgcn_sched_barrier(0); }
;             }
;     __device__ __forceinline__ Pre pre(const Unit& u, int r, int cit) const { const size_t off = (size_t)(u.arow0 + r) * D + u.pn * 256 + cit; return Pre{__builtin_nontemporal_load((const f32x4*)(x + off)), __builtin_nontemporal_load((const f32x4*)(x + off + 4)), __builtin_nontemporal_load((const f3 ...
;     __device__ __forceinline__ void post(const Unit& u, int r, int cit, const float* v0, const float* v1, const Pre& p) const {
;         const size_t off = (size_t)(u.arow0 + r) * D + u.pn * 256 + cit; float a[8], b[8];
; #pragma unroll
;         for (int i = 0; i < 4; ++i) { a[i] = p.a0[i] + v0[i]; a[4 + i] = p.a1[i] + v0[4 + i]; b[i] = p.b0[i] + v1[i]; b[4 + i] = p.b1[i] + v1[4 + i]; }
.LBB0_1257:
	s_nop 1
	v_add_u32_e32 v66, v204, v199
	v_ashrrev_i32_e32 v67, 31, v66
	v_lshlrev_b64 v[66:67], 13, v[66:67]
	v_lshl_add_u64 v[74:75], v[188:189], 0, v[66:67]
	global_load_dwordx4 v[66:69], v[74:75], off offset:16 nt
	global_load_dwordx4 v[70:73], v[74:75], off nt
	v_lshl_add_u64 v[78:79], v[74:75], 0, s[22:23]
	v_add_co_u32_e32 v74, vcc, 0x10000, v74
	s_nop 1
	v_addc_co_u32_e32 v75, vcc, 0, v75, vcc
	global_load_dwordx4 v[74:77], v[74:75], off nt
	s_nop 0
	global_load_dwordx4 v[78:81], v[78:79], off offset:16 nt
	s_nop 0
	v_cndmask_b32_e64 v244, 0, 1, s[20:21]
	v_cmp_ne_u32_e64 s[8:9], 1, v244
	s_andn2_b64 vcc, exec, s[20:21]
	s_cbranch_vccnz .LBB0_1259
	s_waitcnt vmcnt(18)
	v_cndmask_b32_e64 v242, v54, v62, s[0:1]
	v_mov_b32_e32 v243, v173
	s_nop 1
	v_mov_b32_dpp v243, v242 row_ror:8 row_mask:0xf bank_mask:0xf
	v_cndmask_b32_e64 v242, v55, v63, s[0:1]
	v_cndmask_b32_e64 v62, v62, v243, s[0:1]
	v_cndmask_b32_e64 v54, v243, v54, s[0:1]
	v_mov_b32_e32 v243, v173
	s_nop 0
	v_add_f32_e32 v62, v118, v62
	v_mov_b32_dpp v243, v242 row_ror:8 row_mask:0xf bank_mask:0xf
	v_cndmask_b32_e64 v242, v56, v64, s[0:1]
	v_cndmask_b32_e64 v63, v63, v243, s[0:1]
	v_cndmask_b32_e64 v55, v243, v55, s[0:1]
	v_mov_b32_e32 v243, v173
	v_add_f32_e32 v63, v119, v63
	s_nop 0
	v_mov_b32_dpp v243, v242 row_ror:8 row_mask:0xf bank_mask:0xf
	v_cndmask_b32_e64 v242, v57, v65, s[0:1]
	v_cndmask_b32_e64 v64, v64, v243, s[0:1]
	v_cndmask_b32_e64 v56, v243, v56, s[0:1]
	v_mov_b32_e32 v243, v173
	v_add_f32_e32 v64, v120, v64
	s_nop 0
	v_add_f32_e32 v56, v124, v56
	v_mov_b32_dpp v243, v242 row_ror:8 row_mask:0xf bank_mask:0xf
	v_cndmask_b32_e64 v242, v50, v58, s[0:1]
	v_cndmask_b32_e64 v65, v65, v243, s[0:1]
	v_cndmask_b32_e64 v57, v243, v57, s[0:1]
	v_mov_b32_e32 v243, v173
	v_add_f32_e32 v57, v125, v57
	s_nop 0
	v_mov_b32_dpp v243, v242 row_ror:8 row_mask:0xf bank_mask:0xf
	v_cndmask_b32_e64 v242, v51, v59, s[0:1]
	v_cndmask_b32_e64 v58, v58, v243, s[0:1]
	v_cndmask_b32_e64 v50, v243, v50, s[0:1]
	v_mov_b32_e32 v243, v173
	s_nop 0
	v_add_f32_e32 v118, v126, v50
	v_add_u32_e32 v50, s71, v203
	v_mov_b32_dpp v243, v242 row_ror:8 row_mask:0xf bank_mask:0xf
	v_cndmask_b32_e64 v242, v52, v60, s[0:1]
	v_cndmask_b32_e64 v59, v59, v243, s[0:1]
	v_cndmask_b32_e64 v51, v243, v51, s[0:1]
	v_mov_b32_e32 v243, v173
	v_add_f32_e32 v119, v127, v51
	v_ashrrev_i32_e32 v51, 31, v50
	v_mov_b32_dpp v243, v242 row_ror:8 row_mask:0xf bank_mask:0xf
	v_cndmask_b32_e64 v242, v53, v61, s[0:1]
	v_cndmask_b32_e64 v60, v60, v243, s[0:1]
	v_cndmask_b32_e64 v52, v243, v52, s[0:1]
	v_mov_b32_e32 v243, v173
	v_add_f32_e32 v58, v114, v58
	v_add_f32_e32 v59, v115, v59
	v_mov_b32_dpp v243, v242 row_ror:8 row_mask:0xf bank_mask:0xf
	v_cndmask_b32_e64 v61, v61, v243, s[0:1]
	v_cndmask_b32_e64 v53, v243, v53, s[0:1]
	v_add_f32_e32 v60, v116, v60
	v_add_f32_e32 v116, v128, v52
	v_add_f32_e32 v52, v121, v65
	v_add_f32_e32 v61, v117, v61
	v_lshlrev_b64 v[50:51], 12, v[50:51]
	v_add_f32_e32 v114, v122, v54
	v_add_f32_e32 v115, v123, v55
	v_add_f32_e32 v65, v129, v53
	v_lshl_add_u64 v[54:55], v[186:187], 0, v[50:51]
	v_cvt_pk_bf16_f32 v50, v62, v63
	v_cvt_pk_bf16_f32 v51, v64, v52
	v_cvt_pk_bf16_f32 v52, v58, v59
	v_cvt_pk_bf16_f32 v53, v60, v61
	global_store_dwordx4 v[54:55], v[50:53], off
	v_add_co_u32_e32 v54, vcc, 0x8000, v54
	s_nop 0
	v_cvt_pk_bf16_f32 v50, v114, v115
	v_cvt_pk_bf16_f32 v51, v56, v57
	v_cvt_pk_bf16_f32 v52, v118, v119
	v_cvt_pk_bf16_f32 v53, v116, v65
	v_addc_co_u32_e32 v55, vcc, 0, v55, vcc
	global_store_dwordx4 v[54:55], v[50:53], off
.LBB0_1259:
	s_and_b64 vcc, exec, s[8:9]
	s_cbranch_vccnz .LBB0_1261
	s_waitcnt vmcnt(14)
	s_nop 0
	v_cndmask_b32_e64 v242, v38, v46, s[0:1]
	v_mov_b32_e32 v243, v173
	s_nop 1
	v_mov_b32_dpp v243, v242 row_ror:8 row_mask:0xf bank_mask:0xf
	v_cndmask_b32_e64 v242, v39, v47, s[0:1]
	v_cndmask_b32_e64 v46, v46, v243, s[0:1]
	v_cndmask_b32_e64 v38, v243, v38, s[0:1]
	v_mov_b32_e32 v243, v173
	s_nop 0
	v_add_f32_e32 v46, v102, v46
	v_mov_b32_dpp v243, v242 row_ror:8 row_mask:0xf bank_mask:0xf
	v_cndmask_b32_e64 v242, v40, v48, s[0:1]
	v_cndmask_b32_e64 v47, v47, v243, s[0:1]
	v_cndmask_b32_e64 v39, v243, v39, s[0:1]
	v_mov_b32_e32 v243, v173
	v_add_f32_e32 v47, v103, v47
	s_nop 0
	v_mov_b32_dpp v243, v242 row_ror:8 row_mask:0xf bank_mask:0xf
	v_cndmask_b32_e64 v242, v41, v49, s[0:1]
	v_cndmask_b32_e64 v48, v48, v243, s[0:1]
	v_cndmask_b32_e64 v40, v243, v40, s[0:1]
	v_mov_b32_e32 v243, v173
	v_add_f32_e32 v48, v104, v48
	s_nop 0
	v_add_f32_e32 v40, v108, v40
	v_mov_b32_dpp v243, v242 row_ror:8 row_mask:0xf bank_mask:0xf
	v_cndmask_b32_e64 v242, v34, v42, s[0:1]
	v_cndmask_b32_e64 v49, v49, v243, s[0:1]
	v_cndmask_b32_e64 v41, v243, v41, s[0:1]
	v_mov_b32_e32 v243, v173
	v_add_f32_e32 v41, v109, v41
	s_nop 0
	v_mov_b32_dpp v243, v242 row_ror:8 row_mask:0xf bank_mask:0xf
	v_cndmask_b32_e64 v242, v35, v43, s[0:1]
	v_cndmask_b32_e64 v42, v42, v243, s[0:1]
	v_cndmask_b32_e64 v34, v243, v34, s[0:1]
	v_mov_b32_e32 v243, v173
	s_nop 0
	v_add_f32_e32 v102, v110, v34
	v_add_u32_e32 v34, s73, v203
	v_mov_b32_dpp v243, v242 row_ror:8 row_mask:0xf bank_mask:0xf
	v_cndmask_b32_e64 v242, v36, v44, s[0:1]
	v_cndmask_b32_e64 v43, v43, v243, s[0:1]
	v_cndmask_b32_e64 v35, v243, v35, s[0:1]
	v_mov_b32_e32 v243, v173
	v_add_f32_e32 v103, v111, v35
	v_ashrrev_i32_e32 v35, 31, v34
	v_mov_b32_dpp v243, v242 row_ror:8 row_mask:0xf bank_mask:0xf
	v_cndmask_b32_e64 v242, v37, v45, s[0:1]
	v_cndmask_b32_e64 v44, v44, v243, s[0:1]
	v_cndmask_b32_e64 v36, v243, v36, s[0:1]
	v_mov_b32_e32 v243, v173
	v_add_f32_e32 v42, v98, v42
	v_add_f32_e32 v43, v99, v43
	v_mov_b32_dpp v243, v242 row_ror:8 row_mask:0xf bank_mask:0xf
	v_cndmask_b32_e64 v45, v45, v243, s[0:1]
	v_cndmask_b32_e64 v37, v243, v37, s[0:1]
	v_add_f32_e32 v44, v100, v44
	v_add_f32_e32 v100, v112, v36
	v_add_f32_e32 v36, v105, v49
	v_add_f32_e32 v45, v101, v45
	v_lshlrev_b64 v[34:35], 12, v[34:35]
	v_add_f32_e32 v98, v106, v38
	v_add_f32_e32 v99, v107, v39
	v_add_f32_e32 v49, v113, v37
	v_lshl_add_u64 v[38:39], v[186:187], 0, v[34:35]
	v_cvt_pk_bf16_f32 v34, v46, v47
	v_cvt_pk_bf16_f32 v35, v48, v36
	v_cvt_pk_bf16_f32 v36, v42, v43
	v_cvt_pk_bf16_f32 v37, v44, v45
	global_store_dwordx4 v[38:39], v[34:37], off
	v_add_co_u32_e32 v38, vcc, 0x8000, v38
	s_nop 0
	v_cvt_pk_bf16_f32 v34, v98, v99
	v_cvt_pk_bf16_f32 v35, v40, v41
	v_cvt_pk_bf16_f32 v36, v102, v103
	v_cvt_pk_bf16_f32 v37, v100, v49
	v_addc_co_u32_e32 v39, vcc, 0, v39, vcc
	global_store_dwordx4 v[38:39], v[34:37], off
; template <class Epi, class Sched, bool GATHER, bool ALIGN_EPI = true, bool SP2 = true, bool REMAP64 = false>
; __device__ __forceinline__ void gemm_phase(LAS unsigned char* lds, const bf16* Ag, const bf16* Btg, const int K, const Sched& S, const Epi& E) {
;     ...
;             const bool hi = RP && (fr >= 8); const int rsh = hi ? -8 : 0, citx = hi ? cit + 32 : cit;
;             typename Epi::Pre pq[2];
;             { const int r0_ = wr * 64 + fr; pq[0] = E.pre(cur, (r0_ < cur.nrows ? r0_ : cur.nrows - 1) + rsh, citx); }
; #pragma unroll
;             for (int gq = 0; gq < 8; ++gq) { const int ai = gq >> 2, m = gq & 3, r = ai * HALF + wr * 64 + m * 16 + fr;
;                 if (gq + 1 < 8) { const int rn = ((gq + 1) >> 2) * HALF + wr * 64 + ((gq + 1) & 3) * 16 + fr; pq[(gq + 1) & 1] = E.pre(cur, (rn < cur.nrows ? rn : cur.nrows - 1) + rsh, citx); }
;                 __builtin_amdgcn_sched_barrier(0);
;                 if (r < cur.nrows) { float v0[8], v1[8];
; #pragma unroll
;                     for (int i = 0; i < 4; ++i) { v0[i] = acc[ai][0][m][0][i]; v0[4 + i] = acc[ai][0][m][1][i]; v1[i] = acc[ai][1][m][0][i]; v1[4 + i] = acc[ai][1][m][1][i]; }
;                     if constexpr (RP) {
; #pragma unroll
;                         for (int i = 0; i < 8; ++i) { const float snd = hi ? v0[i] : v1[i];
;                             const float rcv = __builtin_bit_cast(float, __builtin_amdgcn_update_dpp(0, __builtin_bit_cast(int, snd), 0x128, 0xf, 0xf, false));
;                             if (hi) v0[i] = rcv; else v1[i] = rcv; } }
;                     E.post(cur, r + rsh, citx, v0, v1, pq[gq & 1]); }
;                 __builtin_amdgcn_sched_barrier(0); }
;             }
;     __device__ __forceinline__ Pre pre(const Unit& u, int r, int cit) const { const size_t off = (size_t)(u.arow0 + r) * D + u.pn * 256 + cit; return Pre{__builtin_nontemporal_load((const f32x4*)(x + off)), __builtin_nontemporal_load((const f32x4*)(x + off + 4)), __builtin_nontemporal_load((const f3 ...
;     __device__ __forceinline__ void post(const Unit& u, int r, int cit, const float* v0, const float* v1, const Pre& p) const {
;         const size_t off = (size_t)(u.arow0 + r) * D + u.pn * 256 + cit; float a[8], b[8];
; #pragma unroll
;         for (int i = 0; i < 4; ++i) { a[i] = p.a0[i] + v0[i]; a[4 + i] = p.a1[i] + v0[4 + i]; b[i] = p.b0[i] + v1[i]; b[4 + i] = p.b1[i] + v1[4 + i]; }
.LBB0_1261:
	s_and_b64 vcc, exec, s[8:9]
	s_cbranch_vccnz .LBB0_1263
	s_waitcnt vmcnt(10)
	s_nop 0
	v_cndmask_b32_e64 v242, v22, v30, s[0:1]
	v_mov_b32_e32 v243, v173
	s_nop 1
	v_mov_b32_dpp v243, v242 row_ror:8 row_mask:0xf bank_mask:0xf
	v_cndmask_b32_e64 v242, v23, v31, s[0:1]
	v_cndmask_b32_e64 v30, v30, v243, s[0:1]
	v_cndmask_b32_e64 v22, v243, v22, s[0:1]
	v_mov_b32_e32 v243, v173
	s_nop 0
	v_add_f32_e32 v30, v86, v30
	v_mov_b32_dpp v243, v242 row_ror:8 row_mask:0xf bank_mask:0xf
	v_cndmask_b32_e64 v242, v24, v32, s[0:1]
	v_cndmask_b32_e64 v31, v31, v243, s[0:1]
	v_cndmask_b32_e64 v23, v243, v23, s[0:1]
	v_mov_b32_e32 v243, v173
	v_add_f32_e32 v31, v87, v31
	s_nop 0
	v_mov_b32_dpp v243, v242 row_ror:8 row_mask:0xf bank_mask:0xf
	v_cndmask_b32_e64 v242, v25, v33, s[0:1]
	v_cndmask_b32_e64 v32, v32, v243, s[0:1]
	v_cndmask_b32_e64 v24, v243, v24, s[0:1]
	v_mov_b32_e32 v243, v173
	v_add_f32_e32 v32, v88, v32
	s_nop 0
	v_add_f32_e32 v24, v92, v24
	v_mov_b32_dpp v243, v242 row_ror:8 row_mask:0xf bank_mask:0xf
	v_cndmask_b32_e64 v242, v18, v26, s[0:1]
	v_cndmask_b32_e64 v33, v33, v243, s[0:1]
	v_cndmask_b32_e64 v25, v243, v25, s[0:1]
	v_mov_b32_e32 v243, v173
	v_add_f32_e32 v25, v93, v25
	s_nop 0
	v_mov_b32_dpp v243, v242 row_ror:8 row_mask:0xf bank_mask:0xf
	v_cndmask_b32_e64 v242, v19, v27, s[0:1]
	v_cndmask_b32_e64 v26, v26, v243, s[0:1]
	v_cndmask_b32_e64 v18, v243, v18, s[0:1]
	v_mov_b32_e32 v243, v173
	s_nop 0
	v_add_f32_e32 v86, v94, v18
	v_add_u32_e32 v18, s74, v203
	v_mov_b32_dpp v243, v242 row_ror:8 row_mask:0xf bank_mask:0xf
	v_cndmask_b32_e64 v242, v20, v28, s[0:1]
	v_cndmask_b32_e64 v27, v27, v243, s[0:1]
	v_cndmask_b32_e64 v19, v243, v19, s[0:1]
	v_mov_b32_e32 v243, v173
	v_add_f32_e32 v87, v95, v19
	v_ashrrev_i32_e32 v19, 31, v18
	v_mov_b32_dpp v243, v242 row_ror:8 row_mask:0xf bank_mask:0xf
	v_cndmask_b32_e64 v242, v21, v29, s[0:1]
	v_cndmask_b32_e64 v28, v28, v243, s[0:1]
	v_cndmask_b32_e64 v20, v243, v20, s[0:1]
	v_mov_b32_e32 v243, v173
	v_add_f32_e32 v26, v82, v26
	v_add_f32_e32 v27, v83, v27
	v_mov_b32_dpp v243, v242 row_ror:8 row_mask:0xf bank_mask:0xf
	v_cndmask_b32_e64 v29, v29, v243, s[0:1]
	v_cndmask_b32_e64 v21, v243, v21, s[0:1]
	v_add_f32_e32 v28, v84, v28
	v_add_f32_e32 v84, v96, v20
	v_add_f32_e32 v20, v89, v33
	v_add_f32_e32 v29, v85, v29
	v_lshlrev_b64 v[18:19], 12, v[18:19]
	v_add_f32_e32 v82, v90, v22
	v_add_f32_e32 v83, v91, v23
	v_add_f32_e32 v33, v97, v21
	v_lshl_add_u64 v[22:23], v[186:187], 0, v[18:19]
	v_cvt_pk_bf16_f32 v18, v30, v31
	v_cvt_pk_bf16_f32 v19, v32, v20
	v_cvt_pk_bf16_f32 v20, v26, v27
	v_cvt_pk_bf16_f32 v21, v28, v29
	global_store_dwordx4 v[22:23], v[18:21], off
	v_add_co_u32_e32 v22, vcc, 0x8000, v22
	s_nop 0
	v_cvt_pk_bf16_f32 v18, v82, v83
	v_cvt_pk_bf16_f32 v19, v24, v25
	v_cvt_pk_bf16_f32 v20, v86, v87
	v_cvt_pk_bf16_f32 v21, v84, v33
	v_addc_co_u32_e32 v23, vcc, 0, v23, vcc
	global_store_dwordx4 v[22:23], v[18:21], off
.LBB0_1263:
	s_and_b64 vcc, exec, s[8:9]
	s_cbranch_vccnz .LBB0_1265
	s_waitcnt vmcnt(6)
	v_cndmask_b32_e64 v18, v6, v14, s[0:1]
	v_mov_b32_e32 v19, v173
	s_nop 1
	v_mov_b32_dpp v19, v18 row_ror:8 row_mask:0xf bank_mask:0xf
	v_cndmask_b32_e64 v18, v7, v15, s[0:1]
	v_cndmask_b32_e64 v14, v14, v19, s[0:1]
	v_cndmask_b32_e64 v6, v19, v6, s[0:1]
	v_mov_b32_e32 v19, v173
	s_nop 0
	v_add_f32_e32 v14, v70, v14
	v_mov_b32_dpp v19, v18 row_ror:8 row_mask:0xf bank_mask:0xf
	v_cndmask_b32_e64 v18, v8, v16, s[0:1]
	v_cndmask_b32_e64 v15, v15, v19, s[0:1]
	v_cndmask_b32_e64 v7, v19, v7, s[0:1]
	v_mov_b32_e32 v19, v173
	v_add_f32_e32 v15, v71, v15
	s_nop 0
	v_add_f32_e32 v20, v75, v7
	v_mov_b32_dpp v19, v18 row_ror:8 row_mask:0xf bank_mask:0xf
	v_cndmask_b32_e64 v18, v9, v17, s[0:1]
	v_cndmask_b32_e64 v16, v16, v19, s[0:1]
	v_cndmask_b32_e64 v8, v19, v8, s[0:1]
	v_mov_b32_e32 v19, v173
	v_add_f32_e32 v16, v72, v16
	v_add_f32_e32 v8, v76, v8
	v_mov_b32_dpp v19, v18 row_ror:8 row_mask:0xf bank_mask:0xf
	v_cndmask_b32_e64 v18, v2, v10, s[0:1]
	v_cndmask_b32_e64 v17, v17, v19, s[0:1]
	v_cndmask_b32_e64 v9, v19, v9, s[0:1]
	v_mov_b32_e32 v19, v173
	v_add_f32_e32 v9, v77, v9
	s_nop 0
	v_mov_b32_dpp v19, v18 row_ror:8 row_mask:0xf bank_mask:0xf
	v_cndmask_b32_e64 v18, v3, v11, s[0:1]
	v_cndmask_b32_e64 v10, v10, v19, s[0:1]
	v_cndmask_b32_e64 v2, v19, v2, s[0:1]
	v_mov_b32_e32 v19, v173
	v_add_f32_e32 v10, v66, v10
	s_nop 0
	v_mov_b32_dpp v19, v18 row_ror:8 row_mask:0xf bank_mask:0xf
	v_cndmask_b32_e64 v18, v4, v12, s[0:1]
	v_cndmask_b32_e64 v11, v11, v19, s[0:1]
	v_cndmask_b32_e64 v3, v19, v3, s[0:1]
	v_mov_b32_e32 v19, v173
	s_nop 0
	v_add_f32_e32 v21, v79, v3
	v_add_f32_e32 v11, v67, v11
	v_mov_b32_dpp v19, v18 row_ror:8 row_mask:0xf bank_mask:0xf
	v_cndmask_b32_e64 v18, v5, v13, s[0:1]
	v_cndmask_b32_e64 v12, v12, v19, s[0:1]
	v_cndmask_b32_e64 v4, v19, v4, s[0:1]
	v_mov_b32_e32 v19, v173
	v_add_f32_e32 v12, v68, v12
	v_add_f32_e32 v22, v80, v4
	v_mov_b32_dpp v19, v18 row_ror:8 row_mask:0xf bank_mask:0xf
	v_cndmask_b32_e64 v13, v13, v19, s[0:1]
	v_cndmask_b32_e64 v5, v19, v5, s[0:1]
	v_add_f32_e32 v19, v78, v2
	v_add_u32_e32 v2, s75, v203
	v_ashrrev_i32_e32 v3, 31, v2
	v_add_f32_e32 v4, v73, v17
	v_add_f32_e32 v13, v69, v13
	v_lshlrev_b64 v[2:3], 12, v[2:3]
	v_add_f32_e32 v18, v74, v6
	v_add_f32_e32 v17, v81, v5
	v_lshl_add_u64 v[6:7], v[186:187], 0, v[2:3]
	v_cvt_pk_bf16_f32 v2, v14, v15
	v_cvt_pk_bf16_f32 v3, v16, v4
	v_cvt_pk_bf16_f32 v4, v10, v11
	v_cvt_pk_bf16_f32 v5, v12, v13
	global_store_dwordx4 v[6:7], v[2:5], off
	v_add_co_u32_e32 v6, vcc, 0x8000, v6
	s_nop 0
	v_cvt_pk_bf16_f32 v2, v18, v20
	v_cvt_pk_bf16_f32 v3, v8, v9
	v_cvt_pk_bf16_f32 v4, v19, v21
	v_cvt_pk_bf16_f32 v5, v22, v17
	v_addc_co_u32_e32 v7, vcc, 0, v7, vcc
	global_store_dwordx4 v[6:7], v[2:5], off

; __global__ void __launch_bounds__(NTHR, 2) fwd(Args args) {
	.amdhsa_kernel _Z3fwd4Args
		.amdhsa_group_segment_fixed_size 0
		.amdhsa_private_segment_fixed_size 0
		.amdhsa_kernarg_size 488
		.amdhsa_user_sgpr_count 2
		.amdhsa_user_sgpr_dispatch_ptr 0
		.amdhsa_user_sgpr_queue_ptr 0
		.amdhsa_user_sgpr_kernarg_segment_ptr 1
		.amdhsa_user_sgpr_dispatch_id 0
		.amdhsa_user_sgpr_kernarg_preload_length 0
		.amdhsa_user_sgpr_kernarg_preload_offset 0
		.amdhsa_user_sgpr_private_segment_size 0
		.amdhsa_uses_dynamic_stack 0
		.amdhsa_enable_private_segment 0
		.amdhsa_system_sgpr_workgroup_id_x 1
		.amdhsa_system_sgpr_workgroup_id_y 0
		.amdhsa_system_sgpr_workgroup_id_z 0
		.amdhsa_system_sgpr_workgroup_info 0
		.amdhsa_system_vgpr_workitem_id 0
		.amdhsa_next_free_vgpr 248
		.amdhsa_next_free_sgpr 98
		.amdhsa_accum_offset 248
		.amdhsa_reserve_vcc 1
		.amdhsa_float_round_mode_32 0
		.amdhsa_float_round_mode_16_64 0
		.amdhsa_float_denorm_mode_32 3
		.amdhsa_float_denorm_mode_16_64 3
		.amdhsa_dx10_clamp 1
		.amdhsa_ieee_mode 1
		.amdhsa_fp16_overflow 0
		.amdhsa_tg_split 0
		.amdhsa_exception_fp_ieee_invalid_op 0
		.amdhsa_exception_fp_denorm_src 0
		.amdhsa_exception_fp_ieee_div_zero 0
		.amdhsa_exception_fp_ieee_overflow 0
		.amdhsa_exception_fp_ieee_underflow 0
		.amdhsa_exception_fp_ieee_inexact 0
		.amdhsa_exception_int_div_zero 0
	.end_amdhsa_kernel

; __global__ void __launch_bounds__(NTHR, 2) fwd(Args args) {
amdhsa.kernels:
  - .agpr_count:     0
    .args:
      - .offset:         0
        .size:           232
        .value_kind:     by_value
      - .offset:         232
        .size:           4
        .value_kind:     hidden_block_count_x
      - .offset:         236
        .size:           4
        .value_kind:     hidden_block_count_y
      - .offset:         240
        .size:           4
        .value_kind:     hidden_block_count_z
      - .offset:         244
        .size:           2
        .value_kind:     hidden_group_size_x
      - .offset:         246
        .size:           2
        .value_kind:     hidden_group_size_y
      - .offset:         248
        .size:           2
        .value_kind:     hidden_group_size_z
      - .offset:         250
        .size:           2
        .value_kind:     hidden_remainder_x
      - .offset:         252
        .size:           2
        .value_kind:     hidden_remainder_y
      - .offset:         254
        .size:           2
        .value_kind:     hidden_remainder_z
      - .offset:         272
        .size:           8
        .value_kind:     hidden_global_offset_x
      - .offset:         280
        .size:           8
        .value_kind:     hidden_global_offset_y
      - .offset:         288
        .size:           8
        .value_kind:     hidden_global_offset_z
      - .offset:         296
        .size:           2
        .value_kind:     hidden_grid_dims
      - .offset:         352
        .size:           4
        .value_kind:     hidden_dynamic_lds_size
    .group_segment_fixed_size: 0
    .kernarg_segment_align: 8
    .kernarg_segment_size: 488
    .language:       OpenCL C
    .language_version:
      - 2
      - 0
    .max_flat_workgroup_size: 512
    .name:           _Z3fwd4Args
    .private_segment_fixed_size: 0
    .sgpr_count:     104
    .sgpr_spill_count: 113
    .symbol:         _Z3fwd4Args.kd
    .uniform_work_group_size: 1
    .uses_dynamic_stack: false
    .vgpr_count:     248
    .vgpr_spill_count: 0
    .wavefront_size: 64
